# speedup vs baseline: 1.0030x; 1.0030x over previous
_Z10cvt_kernelPKfPDF16_lS0_S1_lS0_S1_lS0_S1_lS0_S1_lPjS0_Pf:
	s_cmpk_lt_u32 s2, 0xa0
	s_cbranch_scc1 .Lcvt_orig
	s_sub_u32 s2, s2, 0xa0
	v_lshlrev_b32_e32 v1, 5, v0
	v_lshlrev_b32_e32 v2, 4, v0
	s_cmpk_ge_u32 s2, 0x800
	s_cbranch_scc1 .Lcvt_fw
	s_load_dwordx4 s[4:7], s[0:1], 0x0
	s_lshl_b32 s8, s2, 13
	s_lshl_b32 s9, s2, 12
	s_waitcnt lgkmcnt(0)
	s_add_u32 s4, s4, s8
	s_addc_u32 s5, s5, 0
	s_add_u32 s6, s6, s9
	s_addc_u32 s7, s7, 0
	global_load_dwordx4 v[4:7], v1, s[4:5] nt
	global_load_dwordx4 v[8:11], v1, s[4:5] offset:16 nt
	s_waitcnt vmcnt(1)
	v_cvt_pk_f16_f32 v12, v4, v5
	v_cvt_pk_f16_f32 v13, v6, v7
	s_waitcnt vmcnt(0)
	v_cvt_pk_f16_f32 v14, v8, v9
	v_cvt_pk_f16_f32 v15, v10, v11
	global_store_dwordx4 v2, v[12:15], s[6:7]
	s_endpgm

.LBB0_4:
	s_load_dwordx16 s[36:51], s[0:1], 0x0
	s_add_u32 s2, s2, 0x1000
	s_mov_b32 s3, 0
	s_lshl_b64 s[0:1], s[2:3], 8
	v_or_b32_e32 v4, s0, v0
	v_mov_b32_e32 v5, s1
	s_waitcnt lgkmcnt(0)
	v_cmp_gt_i64_e64 s[2:3], s[40:41], v[4:5]
	v_cmp_le_i64_e32 vcc, s[40:41], v[4:5]
	v_mov_b32_e32 v2, 1.0
	v_mov_b64_e32 v[0:1], s[36:37]
	v_mov_b64_e32 v[6:7], s[38:39]
	s_and_saveexec_b64 s[18:19], vcc
	s_cbranch_execz .LBB0_12
	v_mov_b32_e32 v0, s41
	v_subrev_co_u32_e32 v4, vcc, s40, v4
	v_mov_b64_e32 v[6:7], s[44:45]
	s_nop 0
	v_subb_co_u32_e32 v5, vcc, v5, v0, vcc
	v_cmp_gt_i64_e32 vcc, s[46:47], v[4:5]
	v_cmp_le_i64_e64 s[0:1], s[46:47], v[4:5]
	v_mov_b64_e32 v[0:1], s[42:43]
	s_and_saveexec_b64 s[20:21], s[0:1]
	s_cbranch_execz .LBB0_11
	v_mov_b32_e32 v0, s47
	v_subrev_co_u32_e64 v4, s[0:1], s46, v4
	v_mov_b64_e32 v[6:7], s[50:51]
	s_nop 0
	v_subb_co_u32_e64 v5, s[0:1], v5, v0, s[0:1]
	v_cmp_gt_i64_e64 s[22:23], s[4:5], v[4:5]
	v_cmp_le_i64_e64 s[0:1], s[4:5], v[4:5]
	v_mov_b64_e32 v[0:1], s[48:49]
	s_and_saveexec_b64 s[24:25], s[0:1]
	s_cbranch_execz .LBB0_10
	v_mov_b32_e32 v0, s5
	v_subrev_co_u32_e64 v4, s[0:1], s4, v4
	v_mov_b64_e32 v[6:7], s[8:9]
	s_nop 0
	v_subb_co_u32_e64 v5, s[0:1], v5, v0, s[0:1]
	v_cmp_gt_i64_e64 s[4:5], s[10:11], v[4:5]
	v_cmp_le_i64_e64 s[0:1], s[10:11], v[4:5]
	v_mov_b64_e32 v[0:1], s[6:7]
	s_and_saveexec_b64 s[6:7], s[0:1]
	v_mov_b32_e32 v0, s11
	v_subrev_co_u32_e64 v4, s[0:1], s10, v4
	s_andn2_b64 s[4:5], s[4:5], exec
	s_nop 0
	v_subb_co_u32_e64 v5, s[0:1], v5, v0, s[0:1]
	v_cmp_gt_i64_e64 s[0:1], s[16:17], v[4:5]
	s_and_b64 s[0:1], s[0:1], exec
	v_mov_b64_e32 v[0:1], s[12:13]
	v_mov_b64_e32 v[6:7], s[14:15]
	s_or_b64 s[4:5], s[4:5], s[0:1]
	s_or_b64 exec, exec, s[6:7]
	s_andn2_b64 s[0:1], s[22:23], exec
	s_and_b64 s[4:5], s[4:5], exec
	s_or_b64 s[22:23], s[0:1], s[4:5]
